# P7 K-loop: two of the six LDS-DMA pieces at each of S0/S1 issued between the MFMAs of the following compute segment
# speedup vs baseline: 1.0036x; 1.0036x over previous
; #define PG8_STAGE_B(bufoff, gbase) do { _Pragma("unroll") for (int _i = 0; _i < 2; ++_i) \
;         __builtin_amdgcn_global_load_lds((const unsigned*)((const char*)(gbase) + voffB[_i]), (LAS unsigned*)(lds + (bufoff) + ldsw + _i * 8192), 16, 0, 0); } while (0)
; #define PG8_STAGE_A(bufoff, gbase, VO, h) do { _Pragma("unroll") for (int _i = 0; _i < 2; ++_i) \
;         __builtin_amdgcn_global_load_lds((const unsigned*)((const char*)(gbase) + (VO)[h][_i]), (LAS unsigned*)(lds + (bufoff) + ldsw + _i * 8192), 16, 0, 0); } while (0)
; #define PG8_WAIT_V(n) asm volatile("s_waitcnt vmcnt(" #n ")" ::: "memory")
; #define PG8_WAIT_L(n) asm volatile("s_waitcnt lgkmcnt(" #n ")" ::: "memory")
; #define PG8_WAIT_VX(rx) do { if (rx) asm volatile("s_waitcnt vmcnt(%0)" :: "n"(8 + Epi::NVM) : "memory"); else asm volatile("s_waitcnt vmcnt(8)" ::: "memory"); } while (0)
; #define PG8_BAR __builtin_amdgcn_s_barrier()
; #define PG8_SCHED __builtin_amdgcn_sched_barrier(0)
;     ...
;             PG8_WAIT_VX(rx); PG8_WAIT_L(0); PG8_BAR; PG8_MMA(0, 0, At, B0); PG8_MMA(0, 1, At, B1); PG8_BAR; PG8_SCHED;
;             PG8_LDA(At, 1, 1); PG8_STAGE_B(PG8_SB(1, 0), b3); PG8_STAGE_B(PG8_SB(1, 1), b3 + hstepB); PG8_STAGE_A(PG8_SA(1, 0), a3, vo2, 0);
;             PG8_WAIT_V(8); PG8_WAIT_L(0); PG8_BAR; PG8_MMA(1, 0, At, B0); PG8_MMA(1, 1, At, B1); PG8_BAR; PG8_SCHED;
.LBB0_1410:
	s_xor_b64 s[26:27], s[22:23], -1
	s_waitcnt lgkmcnt(0)
	s_add_u32 s2, s24, 0x40000
	s_addc_u32 s3, s25, 0
	s_barrier
	s_setprio 1
	s_waitcnt lgkmcnt(0)
	v_mfma_scale_f32_16x16x128_f8f6f4 v[190:193], v[24:31], v[56:63], v[190:193], v226, v228 op_sel_hi:[0,0,0]
	v_mfma_scale_f32_16x16x128_f8f6f4 v[186:189], v[16:23], v[56:63], v[186:189], v226, v228 op_sel_hi:[0,0,0]
	v_mfma_scale_f32_16x16x128_f8f6f4 v[178:181], v[24:31], v[48:55], v[178:181], v226, v228 op_sel_hi:[0,0,0]
	v_mfma_scale_f32_16x16x128_f8f6f4 v[170:173], v[16:23], v[48:55], v[170:173], v226, v228 op_sel_hi:[0,0,0]
	v_mfma_scale_f32_16x16x128_f8f6f4 v[162:165], v[24:31], v[40:47], v[162:165], v226, v228 op_sel_hi:[0,0,0]
	v_mfma_scale_f32_16x16x128_f8f6f4 v[154:157], v[16:23], v[40:47], v[154:157], v226, v228 op_sel_hi:[0,0,0]
	v_mfma_scale_f32_16x16x128_f8f6f4 v[146:149], v[24:31], v[32:39], v[146:149], v226, v228 op_sel_hi:[0,0,0]
	v_mfma_scale_f32_16x16x128_f8f6f4 v[138:141], v[16:23], v[32:39], v[138:141], v226, v228 op_sel_hi:[0,0,0]
	s_setprio 0
	s_setprio 1
	v_mfma_scale_f32_16x16x128_f8f6f4 v[182:185], v[8:15], v[56:63], v[182:185], v226, v228 op_sel_hi:[0,0,0]
	v_mfma_scale_f32_16x16x128_f8f6f4 v[174:177], v[0:7], v[56:63], v[174:177], v226, v228 op_sel_hi:[0,0,0]
	v_mfma_scale_f32_16x16x128_f8f6f4 v[166:169], v[8:15], v[48:55], v[166:169], v226, v228 op_sel_hi:[0,0,0]
	v_mfma_scale_f32_16x16x128_f8f6f4 v[158:161], v[0:7], v[48:55], v[158:161], v226, v228 op_sel_hi:[0,0,0]
	v_mfma_scale_f32_16x16x128_f8f6f4 v[150:153], v[8:15], v[40:47], v[150:153], v226, v228 op_sel_hi:[0,0,0]
	v_mfma_scale_f32_16x16x128_f8f6f4 v[142:145], v[0:7], v[40:47], v[142:145], v226, v228 op_sel_hi:[0,0,0]
	v_mfma_scale_f32_16x16x128_f8f6f4 v[134:137], v[8:15], v[32:39], v[134:137], v226, v228 op_sel_hi:[0,0,0]
	v_mfma_scale_f32_16x16x128_f8f6f4 v[130:133], v[0:7], v[32:39], v[130:133], v226, v228 op_sel_hi:[0,0,0]
	s_setprio 0
	s_barrier
	s_mov_b32 m0, s42
	v_lshl_add_u64 v[214:215], s[2:3], 0, v[64:65]
	ds_read_b128 v[32:35], v212 offset:49152
	ds_read_b128 v[36:39], v212 offset:50176
	ds_read_b128 v[40:43], v212 offset:51200
	ds_read_b128 v[44:47], v212 offset:52224
	ds_read_b128 v[48:51], v212 offset:53248
	ds_read_b128 v[52:55], v212 offset:54272
	ds_read_b128 v[56:59], v212 offset:55296
	ds_read_b128 v[60:63], v212 offset:56320
	global_load_lds_dwordx4 v[214:215], off
	v_lshl_add_u64 v[214:215], s[2:3], 0, v[198:199]
	s_add_u32 s2, s24, 0x40200
	s_mov_b32 m0, s43
	s_addc_u32 s3, s25, 0
	global_load_lds_dwordx4 v[214:215], off
	v_lshl_add_u64 v[214:215], s[2:3], 0, v[64:65]
	s_mov_b32 m0, s46
	v_lshl_add_u64 v[206:207], v[206:207], 0, s[94:95]
	global_load_lds_dwordx4 v[214:215], off
	v_lshl_add_u64 v[214:215], s[2:3], 0, v[198:199]
	s_mov_b32 m0, s47
	s_nop 0
	global_load_lds_dwordx4 v[214:215], off
	s_waitcnt vmcnt(6)
	s_waitcnt lgkmcnt(0)
	s_barrier
	s_setprio 1
	s_waitcnt lgkmcnt(0)
	v_mfma_scale_f32_16x16x128_f8f6f4 v[126:129], v[24:31], v[32:39], v[126:129], v226, v228 op_sel_hi:[0,0,0]
	v_mfma_scale_f32_16x16x128_f8f6f4 v[122:125], v[16:23], v[32:39], v[122:125], v226, v228 op_sel_hi:[0,0,0]
	s_mov_b32 m0, s44
	v_mfma_scale_f32_16x16x128_f8f6f4 v[114:117], v[24:31], v[40:47], v[114:117], v226, v228 op_sel_hi:[0,0,0]
	v_mfma_scale_f32_16x16x128_f8f6f4 v[106:109], v[16:23], v[40:47], v[106:109], v226, v228 op_sel_hi:[0,0,0]
	global_load_lds_dwordx4 v[206:207], off
	v_mfma_scale_f32_16x16x128_f8f6f4 v[90:93], v[24:31], v[48:55], v[90:93], v226, v228 op_sel_hi:[0,0,0]
	v_mfma_scale_f32_16x16x128_f8f6f4 v[82:85], v[16:23], v[48:55], v[82:85], v226, v228 op_sel_hi:[0,0,0]
	v_lshl_add_u64 v[206:207], v[208:209], 0, s[94:95]
	v_mfma_scale_f32_16x16x128_f8f6f4 v[70:73], v[24:31], v[56:63], v[70:73], v226, v228 op_sel_hi:[0,0,0]
	v_mfma_scale_f32_16x16x128_f8f6f4 v[66:69], v[16:23], v[56:63], v[66:69], v226, v228 op_sel_hi:[0,0,0]
	s_setprio 0
	s_setprio 1
	v_mfma_scale_f32_16x16x128_f8f6f4 v[118:121], v[8:15], v[32:39], v[118:121], v226, v228 op_sel_hi:[0,0,0]
	v_mfma_scale_f32_16x16x128_f8f6f4 v[110:113], v[0:7], v[32:39], v[110:113], v226, v228 op_sel_hi:[0,0,0]
	s_mov_b32 m0, s45
	v_mfma_scale_f32_16x16x128_f8f6f4 v[94:97], v[8:15], v[40:47], v[94:97], v226, v228 op_sel_hi:[0,0,0]
	v_mfma_scale_f32_16x16x128_f8f6f4 v[86:89], v[0:7], v[40:47], v[86:89], v226, v228 op_sel_hi:[0,0,0]
	global_load_lds_dwordx4 v[206:207], off
	v_mfma_scale_f32_16x16x128_f8f6f4 v[102:105], v[8:15], v[48:55], v[102:105], v226, v228 op_sel_hi:[0,0,0]
	v_mfma_scale_f32_16x16x128_f8f6f4 v[98:101], v[0:7], v[48:55], v[98:101], v226, v228 op_sel_hi:[0,0,0]
	v_mfma_scale_f32_16x16x128_f8f6f4 v[78:81], v[8:15], v[56:63], v[78:81], v226, v228 op_sel_hi:[0,0,0]
	v_mfma_scale_f32_16x16x128_f8f6f4 v[74:77], v[0:7], v[56:63], v[74:77], v226, v228 op_sel_hi:[0,0,0]
	s_setprio 0
	s_barrier
	s_mov_b32 s5, 2
	s_mov_b64 s[22:23], 0
	s_mov_b64 s[2:3], -1
	s_and_b64 vcc, exec, s[26:27]
	s_cbranch_vccnz .LBB0_1423

; #define PG8_STAGE_B(bufoff, gbase) do { _Pragma("unroll") for (int _i = 0; _i < 2; ++_i) \
;         __builtin_amdgcn_global_load_lds((const unsigned*)((const char*)(gbase) + voffB[_i]), (LAS unsigned*)(lds + (bufoff) + ldsw + _i * 8192), 16, 0, 0); } while (0)
; #define PG8_STAGE_A(bufoff, gbase, VO, h) do { _Pragma("unroll") for (int _i = 0; _i < 2; ++_i) \
;         __builtin_amdgcn_global_load_lds((const unsigned*)((const char*)(gbase) + (VO)[h][_i]), (LAS unsigned*)(lds + (bufoff) + ldsw + _i * 8192), 16, 0, 0); } while (0)
; #define PG8_WAIT_L(n) asm volatile("s_waitcnt lgkmcnt(" #n ")" ::: "memory")
; #define PG8_WAIT_VX(rx) do { if (rx) asm volatile("s_waitcnt vmcnt(%0)" :: "n"(8 + Epi::NVM) : "memory"); else asm volatile("s_waitcnt vmcnt(8)" ::: "memory"); } while (0)
; #define PG8_BAR __builtin_amdgcn_s_barrier()
; #define PG8_SCHED __builtin_amdgcn_sched_barrier(0)
;     ...
;             PG8_WAIT_VX(rx); PG8_WAIT_L(0); PG8_BAR; PG8_MMA(0, 0, At, B0); PG8_MMA(0, 1, At, B1); PG8_BAR; PG8_SCHED;
;             PG8_LDA(At, 0, 1); PG8_STAGE_B(PG8_SB(0, 0), b2); PG8_STAGE_B(PG8_SB(0, 1), b2 + hstepB); PG8_STAGE_A(PG8_SA(0, 0), a2, vo2, 0);
;             PG8_WAIT_VX(rx); PG8_WAIT_L(0); PG8_BAR; PG8_MMA(1, 0, At, B0); PG8_MMA(1, 1, At, B1); PG8_BAR; PG8_SCHED;
;             PG8_LDB(B0, 1, 0); PG8_LDB(B1, 1, 1); PG8_SCHED; PG8_LDA(At, 1, 0); PG8_STAGE_A(PG8_SA(0, 1), a2, vo2, 1);
.LBB0_1415:
	s_add_u32 s7, s24, 0x100
	s_addc_u32 s26, s25, 0
	s_and_b64 s[24:25], s[2:3], exec
	s_cselect_b32 s27, s11, s26
	s_cselect_b32 s26, s10, s7
	s_lshl_b32 s5, s5, 18
	s_add_u32 s5, s14, s5
	s_addc_u32 s7, s15, 0
	s_add_u32 s5, s5, 0x80000
	s_addc_u32 s7, s7, 0
	s_waitcnt lgkmcnt(0)
	s_and_b64 s[2:3], s[2:3], exec
	s_cselect_b32 s25, s9, s7
	s_cselect_b32 s24, s8, s5
	s_barrier
	s_setprio 1
	s_waitcnt lgkmcnt(0)
	v_mfma_scale_f32_16x16x128_f8f6f4 v[190:193], v[24:31], v[56:63], v[190:193], v226, v228 op_sel_hi:[0,0,0]
	v_mfma_scale_f32_16x16x128_f8f6f4 v[186:189], v[16:23], v[56:63], v[186:189], v226, v228 op_sel_hi:[0,0,0]
	v_mfma_scale_f32_16x16x128_f8f6f4 v[178:181], v[24:31], v[48:55], v[178:181], v226, v228 op_sel_hi:[0,0,0]
	v_mfma_scale_f32_16x16x128_f8f6f4 v[170:173], v[16:23], v[48:55], v[170:173], v226, v228 op_sel_hi:[0,0,0]
	v_mfma_scale_f32_16x16x128_f8f6f4 v[162:165], v[24:31], v[40:47], v[162:165], v226, v228 op_sel_hi:[0,0,0]
	v_mfma_scale_f32_16x16x128_f8f6f4 v[154:157], v[16:23], v[40:47], v[154:157], v226, v228 op_sel_hi:[0,0,0]
	v_mfma_scale_f32_16x16x128_f8f6f4 v[146:149], v[24:31], v[32:39], v[146:149], v226, v228 op_sel_hi:[0,0,0]
	v_mfma_scale_f32_16x16x128_f8f6f4 v[138:141], v[16:23], v[32:39], v[138:141], v226, v228 op_sel_hi:[0,0,0]
	s_setprio 0
	s_setprio 1
	v_mfma_scale_f32_16x16x128_f8f6f4 v[182:185], v[8:15], v[56:63], v[182:185], v226, v228 op_sel_hi:[0,0,0]
	v_mfma_scale_f32_16x16x128_f8f6f4 v[174:177], v[0:7], v[56:63], v[174:177], v226, v228 op_sel_hi:[0,0,0]
	v_mfma_scale_f32_16x16x128_f8f6f4 v[166:169], v[8:15], v[48:55], v[166:169], v226, v228 op_sel_hi:[0,0,0]
	v_mfma_scale_f32_16x16x128_f8f6f4 v[158:161], v[0:7], v[48:55], v[158:161], v226, v228 op_sel_hi:[0,0,0]
	v_mfma_scale_f32_16x16x128_f8f6f4 v[150:153], v[8:15], v[40:47], v[150:153], v226, v228 op_sel_hi:[0,0,0]
	v_mfma_scale_f32_16x16x128_f8f6f4 v[142:145], v[0:7], v[40:47], v[142:145], v226, v228 op_sel_hi:[0,0,0]
	v_mfma_scale_f32_16x16x128_f8f6f4 v[134:137], v[8:15], v[32:39], v[134:137], v226, v228 op_sel_hi:[0,0,0]
	v_mfma_scale_f32_16x16x128_f8f6f4 v[130:133], v[0:7], v[32:39], v[130:133], v226, v228 op_sel_hi:[0,0,0]
	s_setprio 0
	s_barrier
	s_mov_b32 m0, s35
	v_lshl_add_u64 v[206:207], s[24:25], 0, v[64:65]
	s_add_u32 s2, s24, 0x200
	ds_read_b128 v[56:59], v212 offset:16384
	ds_read_b128 v[60:63], v212 offset:17408
	ds_read_b128 v[48:51], v212 offset:18432
	ds_read_b128 v[52:55], v212 offset:19456
	ds_read_b128 v[40:43], v212 offset:20480
	ds_read_b128 v[44:47], v212 offset:21504
	ds_read_b128 v[32:35], v212 offset:22528
	ds_read_b128 v[36:39], v212 offset:23552
	global_load_lds_dwordx4 v[206:207], off
	v_lshl_add_u64 v[206:207], s[24:25], 0, v[198:199]
	s_mov_b32 m0, s36
	s_addc_u32 s3, s25, 0
	global_load_lds_dwordx4 v[206:207], off
	v_lshl_add_u64 v[206:207], s[2:3], 0, v[64:65]
	s_mov_b32 m0, s37
	v_lshl_add_u64 v[208:209], s[26:27], 0, v[196:197]
	global_load_lds_dwordx4 v[206:207], off
	v_lshl_add_u64 v[206:207], s[2:3], 0, v[198:199]
	s_mov_b32 m0, s38
	v_cndmask_b32_e64 v213, 0, 1, s[28:29]
	global_load_lds_dwordx4 v[206:207], off
	v_lshl_add_u64 v[206:207], s[26:27], 0, v[202:203]
	v_cmp_ne_u32_e64 s[2:3], 1, v213
	s_andn2_b64 vcc, exec, s[28:29]
	s_cbranch_vccnz .LBB0_1420
	s_waitcnt vmcnt(14)
	s_cbranch_execnz .LBB0_1418
.LBB0_1417:
	s_waitcnt vmcnt(6)
.LBB0_1418:
	s_waitcnt lgkmcnt(0)
	s_barrier
	s_setprio 1
	s_waitcnt lgkmcnt(0)
	v_mfma_scale_f32_16x16x128_f8f6f4 v[126:129], v[24:31], v[56:63], v[126:129], v226, v228 op_sel_hi:[0,0,0]
	v_mfma_scale_f32_16x16x128_f8f6f4 v[122:125], v[16:23], v[56:63], v[122:125], v226, v228 op_sel_hi:[0,0,0]
	s_mov_b32 m0, s13
	v_mfma_scale_f32_16x16x128_f8f6f4 v[114:117], v[24:31], v[48:55], v[114:117], v226, v228 op_sel_hi:[0,0,0]
	v_mfma_scale_f32_16x16x128_f8f6f4 v[106:109], v[16:23], v[48:55], v[106:109], v226, v228 op_sel_hi:[0,0,0]
	global_load_lds_dwordx4 v[206:207], off
	v_mfma_scale_f32_16x16x128_f8f6f4 v[90:93], v[24:31], v[40:47], v[90:93], v226, v228 op_sel_hi:[0,0,0]
	v_mfma_scale_f32_16x16x128_f8f6f4 v[82:85], v[16:23], v[40:47], v[82:85], v226, v228 op_sel_hi:[0,0,0]
	v_mfma_scale_f32_16x16x128_f8f6f4 v[70:73], v[24:31], v[32:39], v[70:73], v226, v228 op_sel_hi:[0,0,0]
	v_mfma_scale_f32_16x16x128_f8f6f4 v[66:69], v[16:23], v[32:39], v[66:69], v226, v228 op_sel_hi:[0,0,0]
	s_setprio 0
	s_setprio 1
	v_mfma_scale_f32_16x16x128_f8f6f4 v[118:121], v[8:15], v[56:63], v[118:121], v226, v228 op_sel_hi:[0,0,0]
	v_mfma_scale_f32_16x16x128_f8f6f4 v[110:113], v[0:7], v[56:63], v[110:113], v226, v228 op_sel_hi:[0,0,0]
	s_mov_b32 m0, s39
	v_mfma_scale_f32_16x16x128_f8f6f4 v[94:97], v[8:15], v[48:55], v[94:97], v226, v228 op_sel_hi:[0,0,0]
	v_mfma_scale_f32_16x16x128_f8f6f4 v[86:89], v[0:7], v[48:55], v[86:89], v226, v228 op_sel_hi:[0,0,0]
	global_load_lds_dwordx4 v[208:209], off
	v_mfma_scale_f32_16x16x128_f8f6f4 v[102:105], v[8:15], v[40:47], v[102:105], v226, v228 op_sel_hi:[0,0,0]
	v_mfma_scale_f32_16x16x128_f8f6f4 v[98:101], v[0:7], v[40:47], v[98:101], v226, v228 op_sel_hi:[0,0,0]
	v_mfma_scale_f32_16x16x128_f8f6f4 v[78:81], v[8:15], v[32:39], v[78:81], v226, v228 op_sel_hi:[0,0,0]
	v_mfma_scale_f32_16x16x128_f8f6f4 v[74:77], v[0:7], v[32:39], v[74:77], v226, v228 op_sel_hi:[0,0,0]
	s_setprio 0
	s_barrier
	v_add_u32_e32 v0, 0x18000, v211
	v_add_u32_e32 v4, 0x1c000, v211
	ds_read_b128 v[24:27], v0
	ds_read_b128 v[28:31], v0 offset:1024
	ds_read_b128 v[16:19], v0 offset:2048
	ds_read_b128 v[20:23], v0 offset:3072
	ds_read_b128 v[8:11], v4
	ds_read_b128 v[12:15], v4 offset:1024
	ds_read_b128 v[0:3], v4 offset:2048
	ds_read_b128 v[4:7], v4 offset:3072
	s_mov_b32 m0, s40
	v_lshl_add_u64 v[214:215], s[26:27], 0, v[200:201]
	ds_read_b128 v[56:59], v212 offset:32768
	ds_read_b128 v[60:63], v212 offset:33792
	ds_read_b128 v[48:51], v212 offset:34816
	ds_read_b128 v[52:55], v212 offset:35840
	ds_read_b128 v[40:43], v212 offset:36864
	ds_read_b128 v[44:47], v212 offset:37888
	ds_read_b128 v[32:35], v212 offset:38912
	ds_read_b128 v[36:39], v212 offset:39936
	global_load_lds_dwordx4 v[214:215], off
	v_lshl_add_u64 v[214:215], s[26:27], 0, v[194:195]
	s_mov_b32 m0, s41
	s_and_b64 vcc, exec, s[2:3]
	global_load_lds_dwordx4 v[214:215], off
	s_cbranch_vccnz .LBB0_1421
	s_waitcnt vmcnt(16)
	s_cbranch_execnz .LBB0_1410
	s_branch .LBB0_1422
